# v58 + conv step store section trimmed (scalar token guards, one address base per token pair with offset:2048, cvt_pk rounding)
# speedup vs baseline: 1.0054x; 1.0051x over previous
; __device__ __forceinline__ void ph_conv2(const Params& p, int l, LAS unsigned char* lds, const int wvid) {
;     ...
;             for (int i = 0; i < 38; ++i) x[i] = G[(tl + i) * 256 + c];
; #pragma unroll
;             for (int o = 0; o < 8; ++o) { float acc = cb;
; #pragma unroll
;                 for (int w = 0; w < 31; ++w) acc += wv[w] * x[o + w];
.LBB0_456:
	ds_read2st64_b32 v[40:41], v0 offset1:4
	ds_read2st64_b32 v[38:39], v0 offset0:8 offset1:12
	ds_read2st64_b32 v[36:37], v0 offset0:16 offset1:20
	ds_read2st64_b32 v[34:35], v0 offset0:24 offset1:28
	ds_read2st64_b32 v[32:33], v0 offset0:32 offset1:36
	ds_read2st64_b32 v[30:31], v0 offset0:40 offset1:44
	ds_read2st64_b32 v[28:29], v0 offset0:48 offset1:52
	ds_read2st64_b32 v[26:27], v0 offset0:56 offset1:60
	ds_read2st64_b32 v[24:25], v0 offset0:64 offset1:68
	ds_read2st64_b32 v[22:23], v0 offset0:72 offset1:76
	ds_read2st64_b32 v[20:21], v0 offset0:80 offset1:84
	ds_read2st64_b32 v[18:19], v0 offset0:88 offset1:92
	ds_read2st64_b32 v[16:17], v0 offset0:96 offset1:100
	ds_read2st64_b32 v[14:15], v0 offset0:104 offset1:108
	ds_read2st64_b32 v[12:13], v0 offset0:112 offset1:116
	ds_read2st64_b32 v[10:11], v0 offset0:120 offset1:124
	ds_read2st64_b32 v[8:9], v0 offset0:128 offset1:132
	ds_read2st64_b32 v[6:7], v0 offset0:136 offset1:140
	ds_read2st64_b32 v[4:5], v0 offset0:144 offset1:148
	s_waitcnt lgkmcnt(15)
	v_fma_f32 v120, v60, v40, v55
	v_fmac_f32_e32 v120, v61, v41
	s_waitcnt lgkmcnt(15)
	v_fmac_f32_e32 v120, v62, v38
	v_fmac_f32_e32 v120, v63, v39
	s_waitcnt lgkmcnt(15)
	v_fmac_f32_e32 v120, v64, v36
	v_fmac_f32_e32 v120, v65, v37
	s_waitcnt lgkmcnt(15)
	v_fmac_f32_e32 v120, v66, v34
	v_fmac_f32_e32 v120, v67, v35
	s_waitcnt lgkmcnt(14)
	v_fmac_f32_e32 v120, v68, v32
	v_fmac_f32_e32 v120, v69, v33
	s_waitcnt lgkmcnt(13)
	v_fmac_f32_e32 v120, v70, v30
	v_fmac_f32_e32 v120, v71, v31
	s_waitcnt lgkmcnt(12)
	v_fmac_f32_e32 v120, v72, v28
	v_fmac_f32_e32 v120, v73, v29
	s_waitcnt lgkmcnt(11)
	v_fmac_f32_e32 v120, v74, v26
	v_fmac_f32_e32 v120, v75, v27
	s_waitcnt lgkmcnt(10)
	v_fmac_f32_e32 v120, v76, v24
	v_fmac_f32_e32 v120, v77, v25
	s_waitcnt lgkmcnt(9)
	v_fmac_f32_e32 v120, v78, v22
	v_fmac_f32_e32 v120, v79, v23
	s_waitcnt lgkmcnt(8)
	v_fmac_f32_e32 v120, v80, v20
	v_fmac_f32_e32 v120, v81, v21
	s_waitcnt lgkmcnt(7)
	v_fmac_f32_e32 v120, v82, v18
	v_fmac_f32_e32 v120, v83, v19
	s_waitcnt lgkmcnt(6)
	v_fmac_f32_e32 v120, v84, v16
	v_fmac_f32_e32 v120, v85, v17
	s_waitcnt lgkmcnt(5)
	v_fmac_f32_e32 v120, v86, v14
	v_fmac_f32_e32 v120, v87, v15
	s_waitcnt lgkmcnt(4)
	v_fmac_f32_e32 v120, v88, v12
	v_fmac_f32_e32 v120, v89, v13
	s_waitcnt lgkmcnt(3)
	v_fmac_f32_e32 v120, v90, v10
	v_fma_f32 v121, v60, v41, v55
	v_fmac_f32_e32 v121, v61, v38
	v_fmac_f32_e32 v121, v62, v39
	v_fmac_f32_e32 v121, v63, v36
	v_fmac_f32_e32 v121, v64, v37
	v_fmac_f32_e32 v121, v65, v34
	v_fmac_f32_e32 v121, v66, v35
	v_fmac_f32_e32 v121, v67, v32
	v_fmac_f32_e32 v121, v68, v33
	v_fmac_f32_e32 v121, v69, v30
	v_fmac_f32_e32 v121, v70, v31
	v_fmac_f32_e32 v121, v71, v28
	v_fmac_f32_e32 v121, v72, v29
	v_fmac_f32_e32 v121, v73, v26
	v_fmac_f32_e32 v121, v74, v27
	v_fmac_f32_e32 v121, v75, v24
	v_fmac_f32_e32 v121, v76, v25
	v_fmac_f32_e32 v121, v77, v22
	v_fmac_f32_e32 v121, v78, v23
	v_fmac_f32_e32 v121, v79, v20
	v_fmac_f32_e32 v121, v80, v21
	v_fmac_f32_e32 v121, v81, v18
	v_fmac_f32_e32 v121, v82, v19
	v_fmac_f32_e32 v121, v83, v16
	v_fmac_f32_e32 v121, v84, v17
	v_fmac_f32_e32 v121, v85, v14
	v_fmac_f32_e32 v121, v86, v15
	v_fmac_f32_e32 v121, v87, v12
	v_fmac_f32_e32 v121, v88, v13
	v_fmac_f32_e32 v121, v89, v10
	v_fmac_f32_e32 v121, v90, v11
	v_fma_f32 v122, v60, v38, v55
	v_fmac_f32_e32 v122, v61, v39
	v_fmac_f32_e32 v122, v62, v36
	v_fmac_f32_e32 v122, v63, v37
	v_fmac_f32_e32 v122, v64, v34
	v_fmac_f32_e32 v122, v65, v35
	v_fmac_f32_e32 v122, v66, v32
	v_fmac_f32_e32 v122, v67, v33
	v_fmac_f32_e32 v122, v68, v30
	v_fmac_f32_e32 v122, v69, v31
	v_fmac_f32_e32 v122, v70, v28
	v_fmac_f32_e32 v122, v71, v29
	v_fmac_f32_e32 v122, v72, v26
	v_fmac_f32_e32 v122, v73, v27
	v_fmac_f32_e32 v122, v74, v24
	v_fmac_f32_e32 v122, v75, v25
	v_fmac_f32_e32 v122, v76, v22
	v_fmac_f32_e32 v122, v77, v23
	v_fmac_f32_e32 v122, v78, v20
	v_fmac_f32_e32 v122, v79, v21
	v_fmac_f32_e32 v122, v80, v18
	v_fmac_f32_e32 v122, v81, v19
	v_fmac_f32_e32 v122, v82, v16
	v_fmac_f32_e32 v122, v83, v17
	v_fmac_f32_e32 v122, v84, v14
	v_fmac_f32_e32 v122, v85, v15
	v_fmac_f32_e32 v122, v86, v12
	v_fmac_f32_e32 v122, v87, v13
	v_fmac_f32_e32 v122, v88, v10
	v_fmac_f32_e32 v122, v89, v11
	s_waitcnt lgkmcnt(2)
	v_fmac_f32_e32 v122, v90, v8
	v_fma_f32 v123, v60, v39, v55
	v_fmac_f32_e32 v123, v61, v36
	v_fmac_f32_e32 v123, v62, v37
	v_fmac_f32_e32 v123, v63, v34
	v_fmac_f32_e32 v123, v64, v35
	v_fmac_f32_e32 v123, v65, v32
	v_fmac_f32_e32 v123, v66, v33
	v_fmac_f32_e32 v123, v67, v30
	v_fmac_f32_e32 v123, v68, v31
	v_fmac_f32_e32 v123, v69, v28
	v_fmac_f32_e32 v123, v70, v29
	v_fmac_f32_e32 v123, v71, v26
	v_fmac_f32_e32 v123, v72, v27
	v_fmac_f32_e32 v123, v73, v24
	v_fmac_f32_e32 v123, v74, v25
	v_fmac_f32_e32 v123, v75, v22
	v_fmac_f32_e32 v123, v76, v23
	v_fmac_f32_e32 v123, v77, v20
	v_fmac_f32_e32 v123, v78, v21
	v_fmac_f32_e32 v123, v79, v18
	v_fmac_f32_e32 v123, v80, v19
	v_fmac_f32_e32 v123, v81, v16
	v_fmac_f32_e32 v123, v82, v17
	v_fmac_f32_e32 v123, v83, v14
	v_fmac_f32_e32 v123, v84, v15
	v_fmac_f32_e32 v123, v85, v12
	v_fmac_f32_e32 v123, v86, v13
	v_fmac_f32_e32 v123, v87, v10
	v_fmac_f32_e32 v123, v88, v11
	v_fmac_f32_e32 v123, v89, v8
	v_fmac_f32_e32 v123, v90, v9
	v_fma_f32 v124, v60, v36, v55
	v_fmac_f32_e32 v124, v61, v37
	v_fmac_f32_e32 v124, v62, v34
	v_fmac_f32_e32 v124, v63, v35
	v_fmac_f32_e32 v124, v64, v32
	v_fmac_f32_e32 v124, v65, v33
	v_fmac_f32_e32 v124, v66, v30
	v_fmac_f32_e32 v124, v67, v31
	v_fmac_f32_e32 v124, v68, v28
	v_fmac_f32_e32 v124, v69, v29
	v_fmac_f32_e32 v124, v70, v26
	v_fmac_f32_e32 v124, v71, v27
	v_fmac_f32_e32 v124, v72, v24
	v_fmac_f32_e32 v124, v73, v25
	v_fmac_f32_e32 v124, v74, v22
	v_fmac_f32_e32 v124, v75, v23
	v_fmac_f32_e32 v124, v76, v20
	v_fmac_f32_e32 v124, v77, v21
	v_fmac_f32_e32 v124, v78, v18
	v_fmac_f32_e32 v124, v79, v19
	v_fmac_f32_e32 v124, v80, v16
	v_fmac_f32_e32 v124, v81, v17
	v_fmac_f32_e32 v124, v82, v14
	v_fmac_f32_e32 v124, v83, v15
	v_fmac_f32_e32 v124, v84, v12
	v_fmac_f32_e32 v124, v85, v13
	v_fmac_f32_e32 v124, v86, v10
	v_fmac_f32_e32 v124, v87, v11
	v_fmac_f32_e32 v124, v88, v8
	v_fmac_f32_e32 v124, v89, v9
	s_waitcnt lgkmcnt(1)
; __device__ __forceinline__ void ph_conv2(const Params& p, int l, LAS unsigned char* lds, const int wvid) {
;     ...
;             for (int o = 0; o < 8; ++o) { float acc = cb;
; #pragma unroll
;                 for (int w = 0; w < 31; ++w) acc += wv[w] * x[o + w];
;                 const float mean = wave_sum(acc) * (1.f / 64.f); const float dv = acc - mean; const float var = wave_sum(dv * dv) * (1.f / 64.f);
	v_fmac_f32_e32 v124, v90, v6
	v_fma_f32 v125, v60, v37, v55
	v_fmac_f32_e32 v125, v61, v34
	v_fmac_f32_e32 v125, v62, v35
	v_fmac_f32_e32 v125, v63, v32
	v_fmac_f32_e32 v125, v64, v33
	v_fmac_f32_e32 v125, v65, v30
	v_fmac_f32_e32 v125, v66, v31
	v_fmac_f32_e32 v125, v67, v28
	v_fmac_f32_e32 v125, v68, v29
	v_fmac_f32_e32 v125, v69, v26
	v_fmac_f32_e32 v125, v70, v27
	v_fmac_f32_e32 v125, v71, v24
	v_fmac_f32_e32 v125, v72, v25
	v_fmac_f32_e32 v125, v73, v22
	v_fmac_f32_e32 v125, v74, v23
	v_fmac_f32_e32 v125, v75, v20
	v_fmac_f32_e32 v125, v76, v21
	v_fmac_f32_e32 v125, v77, v18
	v_fmac_f32_e32 v125, v78, v19
	v_fmac_f32_e32 v125, v79, v16
	v_fmac_f32_e32 v125, v80, v17
	v_fmac_f32_e32 v125, v81, v14
	v_fmac_f32_e32 v125, v82, v15
	v_fmac_f32_e32 v125, v83, v12
	v_fmac_f32_e32 v125, v84, v13
	v_fmac_f32_e32 v125, v85, v10
	v_fmac_f32_e32 v125, v86, v11
	v_fmac_f32_e32 v125, v87, v8
	v_fmac_f32_e32 v125, v88, v9
	v_fmac_f32_e32 v125, v89, v6
	v_fmac_f32_e32 v125, v90, v7
	v_fma_f32 v126, v60, v34, v55
	v_fmac_f32_e32 v126, v61, v35
	v_fmac_f32_e32 v126, v62, v32
	v_fmac_f32_e32 v126, v63, v33
	v_fmac_f32_e32 v126, v64, v30
	v_fmac_f32_e32 v126, v65, v31
	v_fmac_f32_e32 v126, v66, v28
	v_fmac_f32_e32 v126, v67, v29
	v_fmac_f32_e32 v126, v68, v26
	v_fmac_f32_e32 v126, v69, v27
	v_fmac_f32_e32 v126, v70, v24
	v_fmac_f32_e32 v126, v71, v25
	v_fmac_f32_e32 v126, v72, v22
	v_fmac_f32_e32 v126, v73, v23
	v_fmac_f32_e32 v126, v74, v20
	v_fmac_f32_e32 v126, v75, v21
	v_fmac_f32_e32 v126, v76, v18
	v_fmac_f32_e32 v126, v77, v19
	v_fmac_f32_e32 v126, v78, v16
	v_fmac_f32_e32 v126, v79, v17
	v_fmac_f32_e32 v126, v80, v14
	v_fmac_f32_e32 v126, v81, v15
	v_fmac_f32_e32 v126, v82, v12
	v_fmac_f32_e32 v126, v83, v13
	v_fmac_f32_e32 v126, v84, v10
	v_fmac_f32_e32 v126, v85, v11
	v_fmac_f32_e32 v126, v86, v8
	v_fmac_f32_e32 v126, v87, v9
	v_fmac_f32_e32 v126, v88, v6
	v_fmac_f32_e32 v126, v89, v7
	s_waitcnt lgkmcnt(0)
	v_fmac_f32_e32 v126, v90, v4
	v_fma_f32 v127, v60, v35, v55
	v_fmac_f32_e32 v127, v61, v32
	v_fmac_f32_e32 v127, v62, v33
	v_fmac_f32_e32 v127, v63, v30
	v_fmac_f32_e32 v127, v64, v31
	v_fmac_f32_e32 v127, v65, v28
	v_fmac_f32_e32 v127, v66, v29
	v_fmac_f32_e32 v127, v67, v26
	v_fmac_f32_e32 v127, v68, v27
	v_fmac_f32_e32 v127, v69, v24
	v_fmac_f32_e32 v127, v70, v25
	v_fmac_f32_e32 v127, v71, v22
	v_fmac_f32_e32 v127, v72, v23
	v_fmac_f32_e32 v127, v73, v20
	v_fmac_f32_e32 v127, v74, v21
	v_fmac_f32_e32 v127, v75, v18
	v_fmac_f32_e32 v127, v76, v19
	v_fmac_f32_e32 v127, v77, v16
	v_fmac_f32_e32 v127, v78, v17
	v_fmac_f32_e32 v127, v79, v14
	v_fmac_f32_e32 v127, v80, v15
	v_fmac_f32_e32 v127, v81, v12
	v_fmac_f32_e32 v127, v82, v13
	v_fmac_f32_e32 v127, v83, v10
	v_fmac_f32_e32 v127, v84, v11
	v_fmac_f32_e32 v127, v85, v8
	v_fmac_f32_e32 v127, v86, v9
	v_fmac_f32_e32 v127, v87, v6
	v_fmac_f32_e32 v127, v88, v7
	v_fmac_f32_e32 v127, v89, v4
	v_fmac_f32_e32 v127, v90, v5
	s_mov_b32 vcc_lo, 0x5a5a5a5a
	s_mov_b32 vcc_hi, 0x5a5a5a5a
	v_cndmask_b32_e32 v136, v121, v120, vcc
	v_cndmask_b32_e32 v137, v123, v122, vcc
	v_cndmask_b32_e32 v138, v125, v124, vcc
	v_cndmask_b32_e32 v139, v127, v126, vcc
	v_cndmask_b32_e32 v140, v120, v121, vcc
	v_cndmask_b32_e32 v141, v122, v123, vcc
	v_cndmask_b32_e32 v142, v124, v125, vcc
	v_cndmask_b32_e32 v143, v126, v127, vcc
	v_add_f32_dpp v144, v136, v140 quad_perm:[1,0,3,2] row_mask:0xf bank_mask:0xf
	v_add_f32_dpp v145, v137, v141 quad_perm:[1,0,3,2] row_mask:0xf bank_mask:0xf
	v_add_f32_dpp v146, v138, v142 quad_perm:[1,0,3,2] row_mask:0xf bank_mask:0xf
	v_add_f32_dpp v147, v139, v143 quad_perm:[1,0,3,2] row_mask:0xf bank_mask:0xf
	s_mov_b32 vcc_lo, 0x3c3c3c3c
	s_mov_b32 vcc_hi, 0x3c3c3c3c
	v_cndmask_b32_e32 v148, v145, v144, vcc
	v_cndmask_b32_e32 v149, v147, v146, vcc
	v_cndmask_b32_e32 v150, v144, v145, vcc
	v_cndmask_b32_e32 v151, v146, v147, vcc
	s_nop 0
	v_add_f32_dpp v136, v148, v150 quad_perm:[2,3,0,1] row_mask:0xf bank_mask:0xf
	v_add_f32_dpp v137, v149, v151 quad_perm:[2,3,0,1] row_mask:0xf bank_mask:0xf
	s_mov_b32 vcc_lo, 0xff00ff00
	s_mov_b32 vcc_hi, 0xff00ff00
	v_cndmask_b32_e32 v138, v137, v136, vcc
	v_cndmask_b32_e32 v139, v136, v137, vcc
	s_nop 1
	v_add_f32_dpp v140, v138, v139 row_ror:8 row_mask:0xf bank_mask:0xf
	s_nop 1
	v_add_f32_dpp v141, v140, v140 row_half_mirror row_mask:0xf bank_mask:0xf
	v_mov_b32_e32 v142, v141
	s_nop 1
	v_permlane16_swap_b32_e32 v141, v142
	v_add_f32_e32 v143, v141, v142
	v_mov_b32_e32 v144, v143
	s_nop 1
	v_permlane32_swap_b32_e32 v143, v144
	v_add_f32_e32 v145, v143, v144
	s_nop 0
	v_readlane_b32 s24, v145, 0
	v_readlane_b32 s25, v145, 1
	v_readlane_b32 s26, v145, 2
	v_readlane_b32 s27, v145, 3
	v_readlane_b32 s28, v145, 8
	v_readlane_b32 s29, v145, 9
	v_readlane_b32 s30, v145, 10
	v_readlane_b32 s31, v145, 11
	v_fmac_f32_e32 v120, s24, v214
	v_fmac_f32_e32 v121, s25, v214
	v_fmac_f32_e32 v122, s26, v214
	v_fmac_f32_e32 v123, s27, v214
	v_fmac_f32_e32 v124, s28, v214
	v_fmac_f32_e32 v125, s29, v214
	v_fmac_f32_e32 v126, s30, v214
	v_fmac_f32_e32 v127, s31, v214
	v_mul_f32_e32 v128, v120, v120
	v_mul_f32_e32 v129, v121, v121
	v_mul_f32_e32 v130, v122, v122
	v_mul_f32_e32 v131, v123, v123
	v_mul_f32_e32 v132, v124, v124
	v_mul_f32_e32 v133, v125, v125
	v_mul_f32_e32 v134, v126, v126
	v_mul_f32_e32 v135, v127, v127
	s_mov_b32 vcc_lo, 0x5a5a5a5a
	s_mov_b32 vcc_hi, 0x5a5a5a5a
	v_cndmask_b32_e32 v136, v129, v128, vcc
	v_cndmask_b32_e32 v137, v131, v130, vcc
	v_cndmask_b32_e32 v138, v133, v132, vcc
	v_cndmask_b32_e32 v139, v135, v134, vcc
; __device__ __forceinline__ bf16_t f2bf(float f) { unsigned u = __float_as_uint(f); u += 0x7FFFu + ((u >> 16) & 1u); return (bf16_t)(u >> 16); }
; __device__ __forceinline__ float frsq(float x) { return __builtin_amdgcn_rsqf(x); }
; __device__ __forceinline__ float sigmoidf_(float x) { return frcp(1.0f + __expf(-x)); }
; __device__ __forceinline__ void ph_conv2(const Params& p, int l, LAS unsigned char* lds, const int wvid) {
;     ...
;                 const float mean = wave_sum(acc) * (1.f / 64.f); const float dv = acc - mean; const float var = wave_sum(dv * dv) * (1.f / 64.f);
;                 const float y = dv * frsq(var + 1e-5f) * gg + gb;
;                 const int tg = t0 + tl + o;
;                 if (tg < LT) MIX[((size_t)b * LT + tg) * D + M_D + c] = f2bf(y * sigmoidf_(y)); }
	v_cndmask_b32_e32 v140, v128, v129, vcc
	v_cndmask_b32_e32 v141, v130, v131, vcc
	v_cndmask_b32_e32 v142, v132, v133, vcc
	v_cndmask_b32_e32 v143, v134, v135, vcc
	v_add_f32_dpp v144, v136, v140 quad_perm:[1,0,3,2] row_mask:0xf bank_mask:0xf
	v_add_f32_dpp v145, v137, v141 quad_perm:[1,0,3,2] row_mask:0xf bank_mask:0xf
	v_add_f32_dpp v146, v138, v142 quad_perm:[1,0,3,2] row_mask:0xf bank_mask:0xf
	v_add_f32_dpp v147, v139, v143 quad_perm:[1,0,3,2] row_mask:0xf bank_mask:0xf
	s_mov_b32 vcc_lo, 0x3c3c3c3c
	s_mov_b32 vcc_hi, 0x3c3c3c3c
	v_cndmask_b32_e32 v148, v145, v144, vcc
	v_cndmask_b32_e32 v149, v147, v146, vcc
	v_cndmask_b32_e32 v150, v144, v145, vcc
	v_cndmask_b32_e32 v151, v146, v147, vcc
	s_nop 0
	v_add_f32_dpp v136, v148, v150 quad_perm:[2,3,0,1] row_mask:0xf bank_mask:0xf
	v_add_f32_dpp v137, v149, v151 quad_perm:[2,3,0,1] row_mask:0xf bank_mask:0xf
	s_mov_b32 vcc_lo, 0xff00ff00
	s_mov_b32 vcc_hi, 0xff00ff00
	v_cndmask_b32_e32 v138, v137, v136, vcc
	v_cndmask_b32_e32 v139, v136, v137, vcc
	s_nop 1
	v_add_f32_dpp v140, v138, v139 row_ror:8 row_mask:0xf bank_mask:0xf
	s_nop 1
	v_add_f32_dpp v141, v140, v140 row_half_mirror row_mask:0xf bank_mask:0xf
	v_mov_b32_e32 v142, v141
	s_nop 1
	v_permlane16_swap_b32_e32 v141, v142
	v_add_f32_e32 v143, v141, v142
	v_mov_b32_e32 v144, v143
	s_nop 1
	v_permlane32_swap_b32_e32 v143, v144
	v_add_f32_e32 v145, v143, v144
	s_nop 0
	v_readlane_b32 s24, v145, 0
	v_readlane_b32 s25, v145, 1
	v_readlane_b32 s26, v145, 2
	v_readlane_b32 s27, v145, 3
	v_readlane_b32 s28, v145, 8
	v_readlane_b32 s29, v145, 9
	v_readlane_b32 s30, v145, 10
	v_readlane_b32 s31, v145, 11
	v_fma_f32 v128, s24, v215, v204
	v_fma_f32 v129, s25, v215, v204
	v_fma_f32 v130, s26, v215, v204
	v_fma_f32 v131, s27, v215, v204
	v_fma_f32 v132, s28, v215, v204
	v_fma_f32 v133, s29, v215, v204
	v_fma_f32 v134, s30, v215, v204
	v_fma_f32 v135, s31, v215, v204
	v_rsq_f32_e32 v128, v128
	v_rsq_f32_e32 v129, v129
	v_rsq_f32_e32 v130, v130
	v_rsq_f32_e32 v131, v131
	v_rsq_f32_e32 v132, v132
	v_rsq_f32_e32 v133, v133
	v_rsq_f32_e32 v134, v134
	v_rsq_f32_e32 v135, v135
	v_mul_f32_e32 v120, v120, v128
	v_mul_f32_e32 v121, v121, v129
	v_mul_f32_e32 v122, v122, v130
	v_mul_f32_e32 v123, v123, v131
	v_mul_f32_e32 v124, v124, v132
	v_mul_f32_e32 v125, v125, v133
	v_mul_f32_e32 v126, v126, v134
	v_mul_f32_e32 v127, v127, v135
	v_fma_f32 v120, v58, v120, v59
	v_fma_f32 v121, v58, v121, v59
	v_fma_f32 v122, v58, v122, v59
	v_fma_f32 v123, v58, v123, v59
	v_fma_f32 v124, v58, v124, v59
	v_fma_f32 v125, v58, v125, v59
	v_fma_f32 v126, v58, v126, v59
	v_fma_f32 v127, v58, v127, v59
	v_mul_f32_e32 v128, 0xbfb8aa3b, v120
	v_mul_f32_e32 v129, 0xbfb8aa3b, v121
	v_mul_f32_e32 v130, 0xbfb8aa3b, v122
	v_mul_f32_e32 v131, 0xbfb8aa3b, v123
	v_mul_f32_e32 v132, 0xbfb8aa3b, v124
	v_mul_f32_e32 v133, 0xbfb8aa3b, v125
	v_mul_f32_e32 v134, 0xbfb8aa3b, v126
	v_mul_f32_e32 v135, 0xbfb8aa3b, v127
	v_exp_f32_e32 v128, v128
	v_exp_f32_e32 v129, v129
	v_exp_f32_e32 v130, v130
	v_exp_f32_e32 v131, v131
	v_exp_f32_e32 v132, v132
	v_exp_f32_e32 v133, v133
	v_exp_f32_e32 v134, v134
	v_exp_f32_e32 v135, v135
	v_add_f32_e32 v128, 1.0, v128
	v_add_f32_e32 v129, 1.0, v129
	v_add_f32_e32 v130, 1.0, v130
	v_add_f32_e32 v131, 1.0, v131
	v_add_f32_e32 v132, 1.0, v132
	v_add_f32_e32 v133, 1.0, v133
	v_add_f32_e32 v134, 1.0, v134
	v_add_f32_e32 v135, 1.0, v135
	v_rcp_f32_e32 v128, v128
	v_rcp_f32_e32 v129, v129
	v_rcp_f32_e32 v130, v130
	v_rcp_f32_e32 v131, v131
	v_rcp_f32_e32 v132, v132
	v_rcp_f32_e32 v133, v133
	v_rcp_f32_e32 v134, v134
	v_rcp_f32_e32 v135, v135
	v_mul_f32_e32 v120, v120, v128
	v_mul_f32_e32 v121, v121, v129
	v_mul_f32_e32 v122, v122, v130
	v_mul_f32_e32 v123, v123, v131
	v_mul_f32_e32 v124, v124, v132
	v_mul_f32_e32 v125, v125, v133
	v_mul_f32_e32 v126, v126, v134
	v_mul_f32_e32 v127, v127, v135
	v_cvt_pk_bf16_f32 v120, v120, v120
	v_cvt_pk_bf16_f32 v121, v121, v121
	v_cvt_pk_bf16_f32 v122, v122, v122
	v_cvt_pk_bf16_f32 v123, v123, v123
	v_cvt_pk_bf16_f32 v124, v124, v124
	v_cvt_pk_bf16_f32 v125, v125, v125
	v_cvt_pk_bf16_f32 v126, v126, v126
	v_cvt_pk_bf16_f32 v127, v127, v127
	v_readfirstlane_b32 s26, v2
	s_mov_b64 s[28:29], 0x1000
	v_mov_b32_e32 v4, v2
	v_ashrrev_i32_e32 v5, 31, v4
	v_lshl_add_u64 v[4:5], s[6:7], 0, v[4:5]
	v_lshlrev_b64 v[4:5], 11, v[4:5]
	v_lshl_add_u64 v[4:5], v[56:57], 0, v[4:5]
	s_add_i32 s27, s26, 0
	s_cmp_lt_i32 s27, s33
	s_cbranch_scc0 .Lcv_st0
	global_store_short v[4:5], v120, off
.Lcv_st0:
	s_add_i32 s27, s26, 1
	s_cmp_lt_i32 s27, s33
	s_cbranch_scc0 .Lcv_st1
	global_store_short v[4:5], v121, off offset:2048
.Lcv_st1:
	v_lshl_add_u64 v[4:5], v[4:5], 0, s[28:29]
	s_add_i32 s27, s26, 2
	s_cmp_lt_i32 s27, s33
	s_cbranch_scc0 .Lcv_st2
	global_store_short v[4:5], v122, off
.Lcv_st2:
	s_add_i32 s27, s26, 3
	s_cmp_lt_i32 s27, s33
	s_cbranch_scc0 .Lcv_st3
	global_store_short v[4:5], v123, off offset:2048
.Lcv_st3:
	v_lshl_add_u64 v[4:5], v[4:5], 0, s[28:29]
	s_add_i32 s27, s26, 4
	s_cmp_lt_i32 s27, s33
	s_cbranch_scc0 .Lcv_st4
	global_store_short v[4:5], v124, off
.Lcv_st4:
	s_add_i32 s27, s26, 5
	s_cmp_lt_i32 s27, s33
	s_cbranch_scc0 .Lcv_st5
	global_store_short v[4:5], v125, off offset:2048
.Lcv_st5:
	v_lshl_add_u64 v[4:5], v[4:5], 0, s[28:29]
	s_add_i32 s27, s26, 6
	s_cmp_lt_i32 s27, s33
	s_cbranch_scc0 .Lcv_st6
	global_store_short v[4:5], v126, off
.Lcv_st6:
	s_add_i32 s27, s26, 7
	s_cmp_lt_i32 s27, s33
	s_cbranch_scc0 .Lcv_st7
	global_store_short v[4:5], v127, off offset:2048
.Lcv_st7:
	s_mov_b64 s[8:9], exec
	s_branch .LBB0_455
